# RG-LRU gate step: column-block roles of waves 4-7 swapped (ni ^= 2) so each SIMD hosts one heavy-epilogue wave and one light wave instead of two heavy ones on SIMDs 0-1
# speedup vs baseline: 1.0126x; 1.0097x over previous
.LBB0_512:
	v_readlane_b32 s24, v254, 18
	s_mov_b64 s[20:21], s[94:95]
	v_mov_b32_e32 v28, v0
	s_cmpk_gt_i32 s24, 0x7f
	s_barrier
	s_cbranch_scc1 .LBB0_562
	s_add_i32 s2, s42, s24
	s_and_b64 s[0:1], s[44:45], exec
	s_movk_i32 s0, 0x1c00
	v_readlane_b32 s19, v253, 55
	v_cmp_gt_i32_e32 vcc, s0, v28
	s_mul_i32 s0, s19, 0x180
	s_waitcnt vmcnt(8)
	v_add_u32_e32 v50, s0, v28
	v_lshlrev_b32_e32 v51, 2, v28
	v_readlane_b32 s0, v253, 16
	v_add_u32_e32 v8, 0xffffff80, v28
	v_mul_hi_i32 v9, v8, s83
	v_add_u32_e32 v53, s0, v51
	s_movk_i32 s0, 0x90
	v_cmp_gt_i32_e64 s[8:9], s0, v28
	v_lshrrev_b32_e32 v10, 31, v9
	s_movk_i32 s0, 0x7f
	v_add_u32_e32 v9, v9, v10
	v_cmp_lt_i32_e64 s[10:11], s0, v28
	v_ashrrev_i32_e32 v11, 3, v28
	s_movk_i32 s0, 0xffe0
	v_bfe_u32 v2, v28, 5, 1
	v_mul_hi_i32 v5, v28, s83
	v_mul_lo_u32 v10, v9, 6
	v_and_b32_e32 v12, 0xffffffe0, v11
	v_bfi_b32 v11, s0, v11, v28
	v_and_b32_e32 v4, 31, v28
	v_lshrrev_b32_e32 v6, 31, v5
	v_sub_u32_e32 v8, v8, v10
	v_bfe_u32 v10, v28, 6, 2
	v_lshrrev_b32_e32 v132, 7, v28
	v_and_b32_e32 v132, 2, v132
	v_xor_b32_e32 v10, v10, v132
	v_mul_lo_u32 v11, v11, s77
	v_lshlrev_b32_e32 v13, 4, v2
	v_add_u32_e32 v30, v5, v6
	v_add3_u32 v55, 0, v11, v13
	v_lshl_or_b32 v11, v10, 5, v4
	v_mul_lo_u32 v7, v30, 6
	v_mul_u32_u24_e32 v11, 0x70, v11
	v_sub_u32_e32 v7, v28, v7
	v_add3_u32 v56, 0, v11, v13
	v_lshrrev_b32_e32 v11, 1, v28
	v_lshlrev_b32_e32 v32, 3, v7
	v_and_or_b32 v4, v11, 32, v4
	v_lshlrev_b32_e32 v11, 4, v7
	v_lshlrev_b32_e32 v7, 5, v7
	v_mul_lo_u32 v14, v30, s91
	v_readlane_b32 s15, v253, 17
	v_add3_u32 v57, 0, v14, v7
	v_ashrrev_i32_e32 v5, 3, v5
	v_mul_lo_u32 v14, v30, s97
	v_lshl_or_b32 v2, v2, 2, v12
	v_add_u32_e32 v5, v5, v6
	v_add3_u32 v62, s15, v11, v14
	v_mul_lo_u32 v11, v2, s91
	v_mul_lo_u32 v2, v2, 48
	v_readlane_b32 s16, v253, 18
	v_mul_lo_u32 v6, v5, 48
	v_or_b32_e32 v2, v2, v4
	v_readlane_b32 s14, v253, 15
	v_cndmask_b32_e64 v36, 0, v9, s[10:11]
	v_add_u32_e32 v13, s16, v7
	v_mul_lo_u32 v7, v9, s97
	v_lshlrev_b32_e32 v9, 2, v4
	v_sub_u32_e32 v6, v28, v6
	v_lshl_add_u32 v67, v2, 2, 0
	v_mul_lo_u32 v2, v5, s93
	v_add_u32_e32 v52, s14, v51
	v_add_u32_e32 v58, s14, v9
	v_readlane_b32 s14, v253, 19
	v_add_lshl_u32 v2, v2, v6, 2
	v_readlane_b32 s17, v253, 20
	v_readlane_b32 s18, v253, 21
	v_add_u32_e32 v68, 0, v2
	v_add_u32_e32 v69, s14, v2
	v_add_u32_e32 v2, 0xc0, v51
	v_add_u32_e32 v77, s17, v2
	v_add_u32_e32 v78, s18, v2
	v_add_u32_e32 v2, 0x180, v51
	v_add_u32_e32 v79, s17, v2
	v_add_u32_e32 v80, s18, v2
	v_add_u32_e32 v2, 0x240, v51
	v_add_u32_e32 v81, s17, v2
	v_add_u32_e32 v82, s18, v2
	v_add_u32_e32 v2, 0x300, v51
	s_load_dwordx2 s[22:23], s[20:21], 0x120
	v_lshlrev_b32_e32 v34, 3, v8
	v_lshl_add_u32 v8, v8, 4, s15
	v_readlane_b32 s15, v253, 22
	v_add_u32_e32 v83, s17, v2
	v_add_u32_e32 v84, s18, v2
	v_add_u32_e32 v2, 0x3c0, v51
	v_add_u32_e32 v63, s15, v51
	v_readlane_b32 s15, v253, 23
	v_add_u32_e32 v85, s17, v2
	v_add_u32_e32 v86, s18, v2
	v_add_u32_e32 v2, 0x480, v51
	s_cselect_b32 s34, s2, 0x100000
	v_cmp_lt_u32_e64 s[2:3], 1, v10
	v_lshrrev_b32_e32 v10, 3, v30
	v_add_u32_e32 v64, s15, v51
	v_readlane_b32 s15, v253, 24
	v_add_u32_e32 v87, s17, v2
	v_add_u32_e32 v88, s18, v2
	v_add_u32_e32 v2, 0x540, v51
	v_ashrrev_i32_e32 v33, 31, v32
	v_add_u32_e32 v9, s14, v9
	v_mul_lo_u32 v10, v10, s91
	s_mul_i32 s36, s19, 0x600
	v_add_u32_e32 v65, s15, v51
	v_readlane_b32 s15, v253, 25
	v_add_u32_e32 v89, s17, v2
	v_add_u32_e32 v90, s18, v2
	v_lshlrev_b32_e32 v2, 1, v28
	v_readlane_b32 s14, v253, 26
	s_lshl_b32 s35, s19, 3
	v_cmp_gt_i32_e64 s[6:7], 48, v28
	v_ashrrev_i32_e32 v29, 31, v28
	v_add_u32_e32 v54, 0, v51
	v_ashrrev_i32_e32 v31, 31, v30
	v_ashrrev_i32_e32 v37, 31, v36
	v_ashrrev_i32_e32 v35, 31, v34
	v_cmp_gt_i32_e64 s[4:5], s93, v28
	v_cmp_gt_i32_e64 s[12:13], s96, v28
	v_cmp_gt_u32_e64 s[0:1], 48, v4
	v_add_u32_e32 v59, s17, v51
	v_add_u32_e32 v60, s18, v51
	v_add_u32_e32 v61, s16, v51
	s_add_i32 s37, s36, 0x480
	v_add_u32_e32 v66, s15, v51
	v_add_u32_e32 v70, 0xc0, v69
	v_add_u32_e32 v71, 0x180, v69
	v_add_u32_e32 v72, 0x240, v69
	v_add_u32_e32 v73, 0x300, v69
	v_add_u32_e32 v74, 0x3c0, v69
	v_add_u32_e32 v75, 0x480, v69
	v_add_u32_e32 v76, 0x540, v69
	s_waitcnt lgkmcnt(0)
	v_lshl_add_u64 v[38:39], v[32:33], 1, s[22:23]
	v_mul_lo_u32 v91, v28, 48
	v_add_u32_e32 v92, s14, v2
	v_add_u32_e32 v93, 0x6240, v2
	v_add_u32_e32 v94, v8, v7
	v_add_u32_e32 v95, v9, v11
	v_add_u32_e32 v96, v13, v10
	s_branch .LBB0_515
